# speedup vs baseline: 1.0085x; 1.0085x over previous
.LBB0_7:
	s_andn2_b64 vcc, exec, s[4:5]
	s_cbranch_vccnz .LBB0_18
	s_load_dwordx4 s[4:7], s[0:1], 0x8
	v_lshl_or_b32 v12, s2, 2, v3
	v_mov_b32_e32 v13, 0
	v_lshlrev_b64 v[4:5], 11, v[12:13]
	v_mov_b32_e32 v3, v13
	s_waitcnt lgkmcnt(0)
	v_lshl_add_u64 v[4:5], s[4:5], 0, v[4:5]
	v_lshl_add_u64 v[2:3], v[4:5], 0, v[2:3]
	global_load_dword v11, v[2:3], off
	global_load_dword v10, v[2:3], off offset:256
	global_load_dword v9, v[2:3], off offset:512
	global_load_dword v8, v[2:3], off offset:768
	global_load_dword v7, v[2:3], off offset:1024
	global_load_dword v6, v[2:3], off offset:1280
	global_load_dword v5, v[2:3], off offset:1536
	global_load_dword v4, v[2:3], off offset:1792
	v_lshlrev_b64 v[2:3], 6, v[12:13]
	v_cmp_eq_u32_e32 vcc, 0, v1
	v_lshl_add_u64 v[2:3], s[6:7], 0, v[2:3]
	s_waitcnt vmcnt(7)
	v_cmp_lt_f32_e64 s[10:11], 0, v11
	s_waitcnt vmcnt(6)
	v_cmp_lt_f32_e64 s[12:13], 0, v10
	s_waitcnt vmcnt(5)
	v_cmp_lt_f32_e64 s[14:15], 0, v9
	s_waitcnt vmcnt(4)
	v_cmp_lt_f32_e64 s[16:17], 0, v8
	s_waitcnt vmcnt(3)
	v_cmp_lt_f32_e64 s[18:19], 0, v7
	s_waitcnt vmcnt(2)
	v_cmp_lt_f32_e64 s[20:21], 0, v6
	s_waitcnt vmcnt(1)
	v_cmp_lt_f32_e64 s[22:23], 0, v5
	s_waitcnt vmcnt(0)
	v_cmp_lt_f32_e64 s[24:25], 0, v4
	v_lshlrev_b32_e32 v16, 3, v1
	v_mov_b32_e32 v17, 0
	v_lshl_add_u64 v[2:3], v[2:3], 0, v[16:17]
	v_writelane_b32 v14, s10, 0
	v_writelane_b32 v15, s11, 0
	v_writelane_b32 v14, s12, 1
	v_writelane_b32 v15, s13, 1
	v_writelane_b32 v14, s14, 2
	v_writelane_b32 v15, s15, 2
	v_writelane_b32 v14, s16, 3
	v_writelane_b32 v15, s17, 3
	v_writelane_b32 v14, s18, 4
	v_writelane_b32 v15, s19, 4
	v_writelane_b32 v14, s20, 5
	v_writelane_b32 v15, s21, 5
	v_writelane_b32 v14, s22, 6
	v_writelane_b32 v15, s23, 6
	v_writelane_b32 v14, s24, 7
	v_writelane_b32 v15, s25, 7
	v_cmp_gt_u32_e32 vcc, 8, v1
	s_and_saveexec_b64 s[4:5], vcc
	global_store_dwordx2 v[2:3], v[14:15], off
	s_or_b64 exec, exec, s[4:5]

.LBB0_19:
	s_load_dwordx2 s[4:5], s[0:1], 0x20
	v_lshl_or_b32 v0, s2, 10, v0
	v_add_u32_e32 v0, 0xfffa0000, v0
	s_mov_b32 s0, 0
	v_ashrrev_i32_e32 v1, 31, v0
	s_waitcnt lgkmcnt(0)
	v_lshl_add_u64 v[0:1], v[0:1], 4, s[4:5]
	s_mov_b32 s2, s0
	s_mov_b32 s3, s0
	s_mov_b32 s1, s0
	v_mov_b64_e32 v[6:7], s[2:3]
	v_add_co_u32_e32 v2, vcc, 0x1000, v0
	v_mov_b64_e32 v[4:5], s[0:1]
	s_nop 0
	v_addc_co_u32_e32 v3, vcc, 0, v1, vcc
	global_store_dwordx4 v[2:3], v[4:7], off
	v_add_co_u32_e32 v2, vcc, 0x2000, v0
	global_store_dwordx4 v[0:1], v[4:7], off
	s_nop 0
	v_addc_co_u32_e32 v3, vcc, 0, v1, vcc
	v_add_co_u32_e32 v0, vcc, 0x3000, v0
	global_store_dwordx4 v[2:3], v[4:7], off
	s_nop 0
	v_addc_co_u32_e32 v1, vcc, 0, v1, vcc
	global_store_dwordx4 v[0:1], v[4:7], off
	s_endpgm
	.section	.rodata,"a",@progbits
	.p2align	6, 0x0
	.amdhsa_kernel _Z7k1_packPKfS0_PmPiP15HIP_vector_typeIfLj4EE
		.amdhsa_group_segment_fixed_size 1024
		.amdhsa_private_segment_fixed_size 0
		.amdhsa_kernarg_size 40
		.amdhsa_user_sgpr_count 2
		.amdhsa_user_sgpr_dispatch_ptr 0
		.amdhsa_user_sgpr_queue_ptr 0
		.amdhsa_user_sgpr_kernarg_segment_ptr 1
		.amdhsa_user_sgpr_dispatch_id 0
		.amdhsa_user_sgpr_kernarg_preload_length 0
		.amdhsa_user_sgpr_kernarg_preload_offset 0
		.amdhsa_user_sgpr_private_segment_size 0
		.amdhsa_uses_dynamic_stack 0
		.amdhsa_enable_private_segment 0
		.amdhsa_system_sgpr_workgroup_id_x 1
		.amdhsa_system_sgpr_workgroup_id_y 0
		.amdhsa_system_sgpr_workgroup_id_z 0
		.amdhsa_system_sgpr_workgroup_info 0
		.amdhsa_system_vgpr_workitem_id 0
		.amdhsa_next_free_vgpr 33
		.amdhsa_next_free_sgpr 26
		.amdhsa_accum_offset 36
		.amdhsa_reserve_vcc 1
		.amdhsa_float_round_mode_32 0
		.amdhsa_float_round_mode_16_64 0
		.amdhsa_float_denorm_mode_32 3
		.amdhsa_float_denorm_mode_16_64 3
		.amdhsa_dx10_clamp 1
		.amdhsa_ieee_mode 1
		.amdhsa_fp16_overflow 0
		.amdhsa_tg_split 0
		.amdhsa_exception_fp_ieee_invalid_op 0
		.amdhsa_exception_fp_denorm_src 0
		.amdhsa_exception_fp_ieee_div_zero 0
		.amdhsa_exception_fp_ieee_overflow 0
		.amdhsa_exception_fp_ieee_underflow 0
		.amdhsa_exception_fp_ieee_inexact 0
		.amdhsa_exception_int_div_zero 0
	.end_amdhsa_kernel

amdhsa.kernels:
  - .agpr_count:     0
    .args:
      - .actual_access:  read_only
        .address_space:  global
        .offset:         0
        .size:           8
        .value_kind:     global_buffer
      - .actual_access:  read_only
        .address_space:  global
        .offset:         8
        .size:           8
        .value_kind:     global_buffer
      - .actual_access:  write_only
        .address_space:  global
        .offset:         16
        .size:           8
        .value_kind:     global_buffer
      - .actual_access:  write_only
        .address_space:  global
        .offset:         24
        .size:           8
        .value_kind:     global_buffer
      - .actual_access:  write_only
        .address_space:  global
        .offset:         32
        .size:           8
        .value_kind:     global_buffer
    .group_segment_fixed_size: 1024
    .kernarg_segment_align: 8
    .kernarg_segment_size: 40
    .language:       OpenCL C
    .language_version:
      - 2
      - 0
    .max_flat_workgroup_size: 256
    .name:           _Z7k1_packPKfS0_PmPiP15HIP_vector_typeIfLj4EE
    .private_segment_fixed_size: 0
    .sgpr_count:     32
    .sgpr_spill_count: 0
    .symbol:         _Z7k1_packPKfS0_PmPiP15HIP_vector_typeIfLj4EE.kd
    .uniform_work_group_size: 1
    .uses_dynamic_stack: false
    .vgpr_count:     33
    .vgpr_spill_count: 0
    .wavefront_size: 64
  - .agpr_count:     0
    .args:
      - .actual_access:  read_only
        .address_space:  global
        .offset:         0
        .size:           8
        .value_kind:     global_buffer
      - .actual_access:  read_only
        .address_space:  global
        .offset:         8
        .size:           8
        .value_kind:     global_buffer
      - .actual_access:  write_only
        .address_space:  global
        .offset:         16
        .size:           8
        .value_kind:     global_buffer
      - .actual_access:  read_only
        .address_space:  global
        .offset:         24
        .size:           8
        .value_kind:     global_buffer
      - .actual_access:  write_only
        .address_space:  global
        .offset:         32
        .size:           8
        .value_kind:     global_buffer
      - .actual_access:  write_only
        .address_space:  global
        .offset:         40
        .size:           8
        .value_kind:     global_buffer
      - .actual_access:  read_only
        .address_space:  global
        .offset:         48
        .size:           8
        .value_kind:     global_buffer
      - .address_space:  global
        .offset:         56
        .size:           8
        .value_kind:     global_buffer
      - .actual_access:  write_only
        .address_space:  global
        .offset:         64
        .size:           8
        .value_kind:     global_buffer
      - .actual_access:  write_only
        .address_space:  global
        .offset:         72
        .size:           8
        .value_kind:     global_buffer
    .group_segment_fixed_size: 34880
    .kernarg_segment_align: 8
    .kernarg_segment_size: 80
    .language:       OpenCL C
    .language_version:
      - 2
      - 0
    .max_flat_workgroup_size: 512
    .name:           _Z7k2_elimPKjPKiPiS2_PfP15HIP_vector_typeIiLj4EEPKfS4_PtSA_
    .private_segment_fixed_size: 0
    .sgpr_count:     54
    .sgpr_spill_count: 0
    .symbol:         _Z7k2_elimPKjPKiPiS2_PfP15HIP_vector_typeIiLj4EEPKfS4_PtSA_.kd
    .uniform_work_group_size: 1
    .uses_dynamic_stack: false
    .vgpr_count:     35
    .vgpr_spill_count: 0
    .wavefront_size: 64
  - .agpr_count:     0
    .args:
      - .actual_access:  read_only
        .address_space:  global
        .offset:         0
        .size:           8
        .value_kind:     global_buffer
      - .actual_access:  read_only
        .address_space:  global
        .offset:         8
        .size:           8
        .value_kind:     global_buffer
      - .actual_access:  read_only
        .address_space:  global
        .offset:         16
        .size:           8
        .value_kind:     global_buffer
      - .actual_access:  read_only
        .address_space:  global
        .offset:         24
        .size:           8
        .value_kind:     global_buffer
      - .actual_access:  read_only
        .address_space:  global
        .offset:         32
        .size:           8
        .value_kind:     global_buffer
      - .actual_access:  read_only
        .address_space:  global
        .offset:         40
        .size:           8
        .value_kind:     global_buffer
      - .actual_access:  write_only
        .address_space:  global
        .offset:         48
        .size:           8
        .value_kind:     global_buffer
    .group_segment_fixed_size: 80064
    .kernarg_segment_align: 8
    .kernarg_segment_size: 56
    .language:       OpenCL C
    .language_version:
      - 2
      - 0
    .max_flat_workgroup_size: 256
    .name:           _Z8k3_chainPKfPK15HIP_vector_typeIiLj4EEPKtS6_S0_S0_Pf
    .private_segment_fixed_size: 0
    .sgpr_count:     28
    .sgpr_spill_count: 0
    .symbol:         _Z8k3_chainPKfPK15HIP_vector_typeIiLj4EEPKtS6_S0_S0_Pf.kd
    .uniform_work_group_size: 1
    .uses_dynamic_stack: false
    .vgpr_count:     184
    .vgpr_spill_count: 0
    .wavefront_size: 64
